# baseline (speedup 1.0000x reference)
.LBB2_13:
	v_exp_f32_e32 v48, v48
	v_exp_f32_e32 v49, v49
	v_mfma_f32_32x32x16_bf16 v[112:127], a[192:195], a[128:131], v[16:31]
	ds_read_b64_tr_b16 v[180:181], v223 offset:0
	v_cvt_pk_bf16_f32 v164, v128, v129
	v_exp_f32_e32 v50, v50
	v_exp_f32_e32 v51, v51
	v_mfma_f32_32x32x16_bf16 v[96:111], a[192:195], a[160:163], v[0:15]
	ds_read_b64_tr_b16 v[182:183], v223 offset:0x800
	v_cvt_pk_bf16_f32 v165, v130, v131
	v_mfma_f32_32x32x16_bf16 v[80:95], a[224:227], a[128:131], v[16:31]
	ds_read_b64_tr_b16 v[184:185], v223 offset:0x200
	v_exp_f32_e32 v236, v52
	v_exp_f32_e32 v237, v53
	v_cvt_pk_bf16_f32 v166, v132, v133
	v_mfma_f32_32x32x16_bf16 v[64:79], a[224:227], a[160:163], v[0:15]
	ds_read_b64_tr_b16 v[186:187], v223 offset:0xa00
	ds_read_b64_tr_b16 v[176:177], v223 offset:0x400
	v_exp_f32_e32 v242, v54
	v_exp_f32_e32 v243, v55
	v_cvt_pk_bf16_f32 v167, v134, v135
	v_exp_f32_e32 v198, v56
	v_exp_f32_e32 v199, v57
	v_mfma_f32_32x32x16_bf16 v[112:127], a[196:199], a[132:135], v[112:127]
	ds_read_b64_tr_b16 v[178:179], v223 offset:0xc00
	v_cvt_pk_bf16_f32 v128, v136, v137
	v_exp_f32_e32 v230, v58
	v_exp_f32_e32 v231, v59
	v_mfma_f32_32x32x16_bf16 v[96:111], a[196:199], a[164:167], v[96:111]
	ds_read_b64_tr_b16 v[188:189], v223 offset:0x600
	v_cvt_pk_bf16_f32 v129, v138, v139
	v_exp_f32_e32 v232, v60
	v_exp_f32_e32 v233, v61
	v_mfma_f32_32x32x16_bf16 v[80:95], a[228:231], a[132:135], v[80:95]
	ds_read_b64_tr_b16 v[190:191], v223 offset:0xe00
	v_cvt_pk_bf16_f32 v130, v140, v141
	v_mfma_f32_32x32x16_bf16 v[64:79], a[228:231], a[164:167], v[64:79]
	ds_read_b64_tr_b16 v[172:173], v223 offset:0x1000
	v_exp_f32_e32 v234, v62
	v_exp_f32_e32 v235, v63
	ds_read_b64_tr_b16 v[174:175], v223 offset:0x1800
	v_cvt_pk_bf16_f32 v131, v142, v143
	v_exp_f32_e32 v141, v32
	v_exp_f32_e32 v142, v33
	v_mfma_f32_32x32x16_bf16 v[112:127], a[200:203], a[136:139], v[112:127]
	ds_read_b64_tr_b16 v[168:169], v223 offset:0x1200
	v_cvt_pk_bf16_f32 v192, v144, v145
	v_exp_f32_e32 v143, v34
	v_mfma_f32_32x32x16_bf16 v[96:111], a[200:203], a[168:171], v[96:111]
	ds_read_b64_tr_b16 v[170:171], v223 offset:0x1a00
	v_exp_f32_e32 v244, v35
	v_cvt_pk_bf16_f32 v193, v146, v147
	v_mfma_f32_32x32x16_bf16 v[80:95], a[232:235], a[136:139], v[80:95]
	ds_read_b64_tr_b16 v[160:161], v223 offset:0x1400
	v_exp_f32_e32 v245, v36
	v_exp_f32_e32 v246, v37
	v_cvt_pk_bf16_f32 v194, v148, v149
	v_mfma_f32_32x32x16_bf16 v[64:79], a[232:235], a[168:171], v[64:79]
	ds_read_b64_tr_b16 v[162:163], v223 offset:0x1c00
	ds_read_b64_tr_b16 v[136:137], v223 offset:0x1600
	v_exp_f32_e32 v247, v38
	v_exp_f32_e32 v248, v39
	v_cvt_pk_bf16_f32 v195, v150, v151
	v_exp_f32_e32 v148, v40
	v_exp_f32_e32 v149, v41
	v_mfma_f32_32x32x16_bf16 v[112:127], a[204:207], a[140:143], v[112:127]
	ds_read_b64_tr_b16 v[138:139], v223 offset:0x1e00
	v_cvt_pk_bf16_f32 v144, v152, v153
	v_exp_f32_e32 v150, v42
	v_exp_f32_e32 v151, v43
	v_mfma_f32_32x32x16_bf16 v[96:111], a[204:207], a[172:175], v[96:111]
	ds_read_b64_tr_b16 v[132:133], v223 offset:0x2000
	v_cvt_pk_bf16_f32 v145, v154, v155
	v_exp_f32_e32 v152, v44
	v_exp_f32_e32 v153, v45
	v_mfma_f32_32x32x16_bf16 v[80:95], a[236:239], a[140:143], v[80:95]
	ds_read_b64_tr_b16 v[134:135], v223 offset:0x2800
	v_cvt_pk_bf16_f32 v146, v156, v157
	v_mfma_f32_32x32x16_bf16 v[64:79], a[236:239], a[172:175], v[64:79]
	ds_read_b64_tr_b16 v[60:61], v223 offset:0x2200
	v_exp_f32_e32 v154, v46
	v_exp_f32_e32 v155, v47
	ds_read_b64_tr_b16 v[62:63], v223 offset:0x2a00
	v_cvt_pk_bf16_f32 v147, v158, v159
	s_mov_b32 s0, s30
	v_mfma_f32_32x32x16_bf16 v[112:127], a[208:211], a[144:147], v[112:127]
	ds_read_b64_tr_b16 v[56:57], v223 offset:0x2400
	v_cvt_pk_bf16_f32 v52, v48, v49
	v_add_f32_e32 v32, v239, v48
	v_add_f32_e32 v33, v238, v49
	s_add_i32 s19, s17, 0xfffda000
	s_mov_b32 s1, s19
	v_mfma_f32_32x32x16_bf16 v[96:111], a[208:211], a[176:179], v[96:111]
	ds_read_b64_tr_b16 v[58:59], v223 offset:0x2c00
	v_cvt_pk_bf16_f32 v53, v50, v51
	v_add_f32_e32 v32, v32, v50
	v_add_f32_e32 v33, v33, v51
	s_mov_b32 s81, s37
	v_mfma_f32_32x32x16_bf16 v[80:95], a[240:243], a[144:147], v[80:95]
	ds_read_b64_tr_b16 v[48:49], v223 offset:0x2600
	v_cvt_pk_bf16_f32 v54, v236, v237
	v_add_f32_e32 v32, v32, v236
	v_add_f32_e32 v33, v33, v237
	s_add_i32 s82, s17, 0xfffdc000
	v_mfma_f32_32x32x16_bf16 v[64:79], a[240:243], a[176:179], v[64:79]
	ds_read_b64_tr_b16 v[50:51], v223 offset:0x2e00
	ds_read_b64_tr_b16 v[44:45], v223 offset:0x3000
	v_cvt_pk_bf16_f32 v55, v242, v243
	v_add_f32_e32 v32, v32, v242
	v_add_f32_e32 v33, v33, v243
	s_mov_b32 s83, s39
	v_mfma_f32_32x32x16_bf16 v[112:127], a[212:215], a[148:151], v[112:127]
	ds_read_b64_tr_b16 v[46:47], v223 offset:0x3800
	v_add_f32_e32 v32, v32, v198
	v_add_f32_e32 v33, v33, v199
	s_add_i32 s24, s17, 0xfffde000
	s_mov_b32 s84, s24
	v_mfma_f32_32x32x16_bf16 v[96:111], a[212:215], a[180:183], v[96:111]
	ds_read_b64_tr_b16 v[40:41], v223 offset:0x3200
	v_add_f32_e32 v32, v32, v230
	v_add_f32_e32 v33, v33, v231
	s_mov_b32 s85, s41
	v_mfma_f32_32x32x16_bf16 v[80:95], a[244:247], a[148:151], v[80:95]
	ds_read_b64_tr_b16 v[42:43], v223 offset:0x3a00
	v_add_f32_e32 v32, v32, v232
	v_add_f32_e32 v33, v33, v233
	s_add_i32 s86, s17, 0xfffe0000
	v_mfma_f32_32x32x16_bf16 v[64:79], a[244:247], a[180:183], v[64:79]
	ds_read_b64_tr_b16 v[36:37], v223 offset:0x3400
	ds_read_b64_tr_b16 v[38:39], v223 offset:0x3c00
	v_add_f32_e32 v156, v32, v234
	v_add_f32_e32 v157, v33, v235
	s_mov_b32 s87, s43
	v_mfma_f32_32x32x16_bf16 v[112:127], a[216:219], a[152:155], v[112:127]
	ds_read_b64_tr_b16 v[32:33], v223 offset:0x3600
	v_cvt_pk_bf16_f32 v140, v141, v142
	v_add_f32_e32 v158, v240, v141
	v_add_f32_e32 v142, v241, v142
	s_add_i32 s88, s17, 0xfffba000
	v_mfma_f32_32x32x16_bf16 v[96:111], a[216:219], a[184:187], v[96:111]
	ds_read_b64_tr_b16 v[34:35], v223 offset:0x3e00
	v_cvt_pk_bf16_f32 v141, v143, v244
	v_add_f32_e32 v143, v158, v143
	v_add_f32_e32 v158, v142, v244
	v_mfma_f32_32x32x16_bf16 v[80:95], a[248:251], a[152:155], v[80:95]
	s_mov_b32 s89, s45
	v_cvt_pk_bf16_f32 v142, v245, v246
	v_add_f32_e32 v159, v143, v245
	v_add_f32_e32 v158, v158, v246
	v_mfma_f32_32x32x16_bf16 v[64:79], a[248:251], a[184:187], v[64:79]
	s_add_i32 s90, s17, 0xfffba080
	v_cvt_pk_bf16_f32 v143, v247, v248
	v_add_f32_e32 v159, v159, v247
	v_add_f32_e32 v158, v158, v248
	v_mfma_f32_32x32x16_bf16 v[112:127], a[220:223], a[156:159], v[112:127]
	s_mov_b32 s91, s47
	v_add_f32_e32 v159, v159, v148
	v_add_f32_e32 v158, v158, v149
	v_mfma_f32_32x32x16_bf16 v[96:111], a[220:223], a[188:191], v[96:111]
	s_add_i32 s92, s17, 0xfffbe000
	v_add_f32_e32 v159, v159, v150
	v_add_f32_e32 v158, v158, v151
	v_mfma_f32_32x32x16_bf16 v[80:95], a[252:255], a[156:159], v[80:95]
	s_mov_b32 s93, s49
	v_add_f32_e32 v159, v159, v152
	v_add_f32_e32 v158, v158, v153
	v_mfma_f32_32x32x16_bf16 v[64:79], a[252:255], a[188:191], v[64:79]
	s_add_i32 s94, s17, 0xfffbe080
	v_add_f32_e32 v159, v159, v154
	v_add_f32_e32 v158, v158, v155
	v_add_f32_e32 v156, v156, v157
	s_waitcnt vmcnt(0) lgkmcnt(0)
	s_barrier
	v_add_f32_e32 v158, v159, v158
	v_mov_b32_e32 v157, v156
	v_mov_b32_e32 v159, v158
	s_nop 0
	v_permlane32_swap_b32_e32 v156, v157
	v_permlane32_swap_b32_e32 v158, v159
	v_add_f32_e32 v156, v156, v157
	v_add_f32_e32 v158, v158, v159
	v_add_f32_e32 v197, v197, v156
	v_add_f32_e32 v196, v196, v158
	s_mov_b32 m0, s0
	v_mfma_f32_32x32x16_bf16 a[0:15], v[180:183], v[164:167], a[0:15]
	buffer_load_dwordx4 v209, s[4:7], s1 offen lds
	s_mov_b32 m0, s81
	v_mfma_f32_32x32x16_bf16 a[16:31], v[180:183], v[192:195], a[16:31]
	buffer_load_dwordx4 v210, s[4:7], s82 offen lds
	s_mov_b32 m0, s83
	v_mfma_f32_32x32x16_bf16 a[32:47], v[184:187], v[164:167], a[32:47]
	buffer_load_dwordx4 v209, s[4:7], s84 offen lds
	s_mov_b32 m0, s85
	v_mfma_f32_32x32x16_bf16 a[48:63], v[184:187], v[192:195], a[48:63]
	buffer_load_dwordx4 v210, s[4:7], s86 offen lds
	s_mov_b32 m0, s87
	v_mfma_f32_32x32x16_bf16 a[64:79], v[176:179], v[164:167], a[64:79]
	buffer_load_dwordx4 v211, s[20:23], s88 offen lds
	s_mov_b32 m0, s89
	v_mfma_f32_32x32x16_bf16 a[80:95], v[176:179], v[192:195], a[80:95]
	buffer_load_dwordx4 v211, s[20:23], s90 offen lds
	s_mov_b32 m0, s91
	v_mfma_f32_32x32x16_bf16 a[96:111], v[188:191], v[164:167], a[96:111]
	buffer_load_dwordx4 v211, s[20:23], s92 offen lds
	s_mov_b32 m0, s93
	v_mfma_f32_32x32x16_bf16 a[112:127], v[188:191], v[192:195], a[112:127]
	buffer_load_dwordx4 v211, s[20:23], s94 offen lds
	v_mfma_f32_32x32x16_bf16 a[0:15], v[172:175], v[128:131], a[0:15]
	v_max3_f32 v156, v112, v113, v80
	v_max3_f32 v157, v114, v115, v81
	v_max3_f32 v156, v156, v82, v83
	v_mfma_f32_32x32x16_bf16 a[16:31], v[172:175], v[144:147], a[16:31]
	ds_read_b128 a[192:195], v219 offset:0
	v_max3_f32 v156, v156, v116, v117
	v_max3_f32 v157, v157, v118, v119
	v_max3_f32 v156, v156, v84, v85
	v_max3_f32 v157, v157, v86, v87
	v_mfma_f32_32x32x16_bf16 a[32:47], v[168:171], v[128:131], a[32:47]
	ds_read_b128 a[196:199], v220 offset:0
	v_max3_f32 v156, v156, v120, v121
	v_max3_f32 v157, v157, v122, v123
	v_max3_f32 v156, v156, v88, v89
	v_max3_f32 v157, v157, v90, v91
	v_mfma_f32_32x32x16_bf16 a[48:63], v[168:171], v[144:147], a[48:63]
	ds_read_b128 a[200:203], v221 offset:0
	v_max3_f32 v156, v156, v124, v125
	v_max3_f32 v157, v157, v126, v127
	v_max3_f32 v156, v156, v92, v93
	v_max3_f32 v157, v157, v94, v95
	v_mfma_f32_32x32x16_bf16 a[64:79], v[160:163], v[128:131], a[64:79]
	ds_read_b128 a[204:207], v222 offset:0
	v_max3_f32 v158, v96, v97, v64
	v_max3_f32 v159, v98, v99, v65
	v_max3_f32 v158, v158, v66, v67
	v_mfma_f32_32x32x16_bf16 a[80:95], v[160:163], v[144:147], a[80:95]
	ds_read_b128 a[208:211], v219 offset:128
	v_max3_f32 v158, v158, v100, v101
	v_max3_f32 v159, v159, v102, v103
	v_max3_f32 v158, v158, v68, v69
	v_max3_f32 v159, v159, v70, v71
	v_mfma_f32_32x32x16_bf16 a[96:111], v[136:139], v[128:131], a[96:111]
	ds_read_b128 a[212:215], v220 offset:128
	v_max3_f32 v128, v158, v104, v105
	v_max3_f32 v129, v159, v106, v107
	v_max3_f32 v128, v128, v72, v73
	v_max3_f32 v129, v129, v74, v75
	v_mfma_f32_32x32x16_bf16 a[112:127], v[136:139], v[144:147], a[112:127]
	ds_read_b128 a[216:219], v221 offset:128
	v_max3_f32 v128, v128, v108, v109
	v_max3_f32 v129, v129, v110, v111
	v_max3_f32 v128, v128, v76, v77
	v_max3_f32 v130, v129, v78, v79
	v_mfma_f32_32x32x16_bf16 a[0:15], v[132:135], v[52:55], a[0:15]
	ds_read_b128 a[220:223], v222 offset:128
	v_max_f32_e32 v129, v156, v157
	v_max_f32_e32 v128, v128, v130
	v_mov_b32_e32 v131, v129
	v_mov_b32_e32 v130, v128
	v_mfma_f32_32x32x16_bf16 a[16:31], v[132:135], v[140:143], a[16:31]
	ds_read_b128 a[224:227], v219 offset:8192
	v_permlane32_swap_b32_e32 v129, v131
	v_permlane32_swap_b32_e32 v128, v130
	v_max_f32_e32 v129, v129, v131
	v_max_f32_e32 v128, v128, v130
	v_max_f32_e32 v130, v129, v128
	v_mfma_f32_32x32x16_bf16 a[32:47], v[60:63], v[52:55], a[32:47]
	ds_read_b128 a[228:231], v220 offset:8192
	v_cmp_lt_f32_e32 vcc, s79, v130
	s_cmp_lg_u64 vcc, 0
	s_cselect_b64 s[0:1], -1, 0
	s_cbranch_vccnz .LBB2_18
.LBB2_14:
	v_cvt_pk_bf16_f32 v156, v198, v199
	v_cvt_pk_bf16_f32 v157, v230, v231
	v_cvt_pk_bf16_f32 v158, v232, v233
	v_cvt_pk_bf16_f32 v159, v234, v235
	v_cvt_pk_bf16_f32 v160, v148, v149
	v_cvt_pk_bf16_f32 v161, v150, v151
	v_cvt_pk_bf16_f32 v162, v152, v153
	v_cvt_pk_bf16_f32 v163, v154, v155
	v_exp_f32_e32 v128, v112
	v_exp_f32_e32 v129, v113
	v_mfma_f32_32x32x16_bf16 a[48:63], v[60:63], v[140:143], a[48:63]
	ds_read_b128 a[232:235], v221 offset:8192
	v_exp_f32_e32 v130, v114
	v_exp_f32_e32 v131, v115
	v_mfma_f32_32x32x16_bf16 a[64:79], v[56:59], v[52:55], a[64:79]
	ds_read_b128 a[236:239], v222 offset:8192
	v_add_f32_e32 v60, v201, v128
	v_add_f32_e32 v61, v201, v129
	v_exp_f32_e32 v132, v116
	v_exp_f32_e32 v133, v117
	v_exp_f32_e32 v134, v118
	v_mfma_f32_32x32x16_bf16 a[80:95], v[56:59], v[140:143], a[80:95]
	ds_read_b128 a[240:243], v219 offset:8320
	v_add_f32_e32 v56, v60, v130
	v_add_f32_e32 v57, v61, v131
	v_exp_f32_e32 v135, v119
	v_exp_f32_e32 v136, v120
	v_mfma_f32_32x32x16_bf16 a[96:111], v[48:51], v[52:55], a[96:111]
	ds_read_b128 a[244:247], v220 offset:8320
	v_add_f32_e32 v52, v56, v132
	v_add_f32_e32 v53, v57, v133
	v_add_f32_e32 v52, v52, v134
	v_exp_f32_e32 v137, v121
	v_exp_f32_e32 v138, v122
	v_exp_f32_e32 v139, v123
	v_mfma_f32_32x32x16_bf16 a[112:127], v[48:51], v[140:143], a[112:127]
	ds_read_b128 a[248:251], v221 offset:8320
	v_add_f32_e32 v48, v53, v135
	v_add_f32_e32 v49, v52, v136
	v_exp_f32_e32 v140, v124
	v_exp_f32_e32 v141, v125
	v_mfma_f32_32x32x16_bf16 a[0:15], v[44:47], v[156:159], a[0:15]
	ds_read_b128 a[252:255], v222 offset:8320
	v_add_f32_e32 v48, v48, v137
	v_add_f32_e32 v49, v49, v138
	v_add_f32_e32 v48, v48, v139
	v_exp_f32_e32 v142, v126
	v_exp_f32_e32 v143, v127
	v_exp_f32_e32 v144, v96
	v_mfma_f32_32x32x16_bf16 a[16:31], v[44:47], v[160:163], a[16:31]
	v_add_f32_e32 v44, v49, v140
	v_add_f32_e32 v45, v48, v141
	v_exp_f32_e32 v145, v97
	v_exp_f32_e32 v146, v98
	v_mfma_f32_32x32x16_bf16 a[32:47], v[40:43], v[156:159], a[32:47]
	v_add_f32_e32 v237, v44, v142
	v_add_f32_e32 v236, v45, v143
	v_add_f32_e32 v44, v201, v144
	v_exp_f32_e32 v147, v99
	v_exp_f32_e32 v148, v100
	v_exp_f32_e32 v149, v101
	v_mfma_f32_32x32x16_bf16 a[48:63], v[40:43], v[160:163], a[48:63]
	v_add_f32_e32 v40, v201, v145
	v_add_f32_e32 v41, v44, v146
	v_exp_f32_e32 v150, v102
	v_exp_f32_e32 v151, v103
	v_mfma_f32_32x32x16_bf16 a[64:79], v[36:39], v[156:159], a[64:79]
	v_add_f32_e32 v40, v40, v147
	v_add_f32_e32 v41, v41, v148
	v_add_f32_e32 v40, v40, v149
	v_exp_f32_e32 v152, v104
	v_exp_f32_e32 v153, v105
	v_exp_f32_e32 v154, v106
	v_mfma_f32_32x32x16_bf16 a[80:95], v[36:39], v[160:163], a[80:95]
	v_add_f32_e32 v36, v41, v150
	v_add_f32_e32 v37, v40, v151
	v_mfma_f32_32x32x16_bf16 a[96:111], v[32:35], v[156:159], a[96:111]
	v_exp_f32_e32 v155, v107
	v_exp_f32_e32 v156, v108
	v_add_f32_e32 v36, v36, v152
	v_add_f32_e32 v37, v37, v153
	v_add_f32_e32 v36, v36, v154
	v_exp_f32_e32 v157, v109
	v_exp_f32_e32 v158, v110
	v_exp_f32_e32 v159, v111
	v_mfma_f32_32x32x16_bf16 a[112:127], v[32:35], v[160:163], a[112:127]
	v_add_f32_e32 v32, v37, v155
	v_add_f32_e32 v33, v36, v156
	s_andn2_b64 vcc, exec, s[0:1]
	v_add_f32_e32 v32, v32, v157
	v_add_f32_e32 v238, v33, v158
	s_nop 0
	v_add_f32_e32 v239, v32, v159
	s_cbranch_vccz .LBB2_19
.LBB2_15:
	s_waitcnt lgkmcnt(0)
	v_exp_f32_e32 v80, v80
	v_exp_f32_e32 v81, v81
	v_mfma_f32_32x32x16_bf16 v[112:127], a[192:195], a[128:131], v[16:31]
	ds_read_b64_tr_b16 v[180:181], v208 offset:0
	v_cvt_pk_bf16_f32 v164, v128, v129
	v_exp_f32_e32 v82, v82
	v_exp_f32_e32 v83, v83
	v_mfma_f32_32x32x16_bf16 v[96:111], a[192:195], a[160:163], v[0:15]
	ds_read_b64_tr_b16 v[182:183], v208 offset:0x800
	v_cvt_pk_bf16_f32 v165, v130, v131
	v_mfma_f32_32x32x16_bf16 v[48:63], a[224:227], a[128:131], v[16:31]
	ds_read_b64_tr_b16 v[184:185], v208 offset:0x200
	v_exp_f32_e32 v240, v84
	v_exp_f32_e32 v241, v85
	v_cvt_pk_bf16_f32 v166, v132, v133
	v_mfma_f32_32x32x16_bf16 v[32:47], a[224:227], a[160:163], v[0:15]
	ds_read_b64_tr_b16 v[186:187], v208 offset:0xa00
	ds_read_b64_tr_b16 v[176:177], v208 offset:0x400
	v_exp_f32_e32 v242, v86
	v_exp_f32_e32 v243, v87
	v_cvt_pk_bf16_f32 v167, v134, v135
	v_exp_f32_e32 v198, v88
	v_exp_f32_e32 v199, v89
	v_mfma_f32_32x32x16_bf16 v[112:127], a[196:199], a[132:135], v[112:127]
	ds_read_b64_tr_b16 v[178:179], v208 offset:0xc00
	v_cvt_pk_bf16_f32 v128, v136, v137
	v_exp_f32_e32 v230, v90
	v_exp_f32_e32 v231, v91
	v_mfma_f32_32x32x16_bf16 v[96:111], a[196:199], a[164:167], v[96:111]
	ds_read_b64_tr_b16 v[188:189], v208 offset:0x600
	v_cvt_pk_bf16_f32 v129, v138, v139
	v_exp_f32_e32 v232, v92
	v_exp_f32_e32 v233, v93
	v_mfma_f32_32x32x16_bf16 v[48:63], a[228:231], a[132:135], v[48:63]
	ds_read_b64_tr_b16 v[190:191], v208 offset:0xe00
	v_cvt_pk_bf16_f32 v130, v140, v141
	v_mfma_f32_32x32x16_bf16 v[32:47], a[228:231], a[164:167], v[32:47]
	ds_read_b64_tr_b16 v[172:173], v208 offset:0x1000
	v_exp_f32_e32 v234, v94
	v_exp_f32_e32 v235, v95
	ds_read_b64_tr_b16 v[174:175], v208 offset:0x1800
	v_cvt_pk_bf16_f32 v131, v142, v143
	v_exp_f32_e32 v141, v64
	v_exp_f32_e32 v142, v65
	v_mfma_f32_32x32x16_bf16 v[112:127], a[200:203], a[136:139], v[112:127]
	ds_read_b64_tr_b16 v[168:169], v208 offset:0x1200
	v_cvt_pk_bf16_f32 v192, v144, v145
	v_exp_f32_e32 v143, v66
	v_mfma_f32_32x32x16_bf16 v[96:111], a[200:203], a[168:171], v[96:111]
	ds_read_b64_tr_b16 v[170:171], v208 offset:0x1a00
	v_exp_f32_e32 v244, v67
	v_cvt_pk_bf16_f32 v193, v146, v147
	v_mfma_f32_32x32x16_bf16 v[48:63], a[232:235], a[136:139], v[48:63]
	ds_read_b64_tr_b16 v[160:161], v208 offset:0x1400
	v_exp_f32_e32 v245, v68
	v_exp_f32_e32 v246, v69
	v_cvt_pk_bf16_f32 v194, v148, v149
	v_mfma_f32_32x32x16_bf16 v[32:47], a[232:235], a[168:171], v[32:47]
	ds_read_b64_tr_b16 v[162:163], v208 offset:0x1c00
	ds_read_b64_tr_b16 v[136:137], v208 offset:0x1600
	v_exp_f32_e32 v247, v70
	v_exp_f32_e32 v248, v71
	v_cvt_pk_bf16_f32 v195, v150, v151
	v_exp_f32_e32 v148, v72
	v_exp_f32_e32 v149, v73
	v_mfma_f32_32x32x16_bf16 v[112:127], a[204:207], a[140:143], v[112:127]
	ds_read_b64_tr_b16 v[138:139], v208 offset:0x1e00
	v_cvt_pk_bf16_f32 v144, v152, v153
	v_exp_f32_e32 v150, v74
	v_exp_f32_e32 v151, v75
	v_mfma_f32_32x32x16_bf16 v[96:111], a[204:207], a[172:175], v[96:111]
	ds_read_b64_tr_b16 v[132:133], v208 offset:0x2000
	v_cvt_pk_bf16_f32 v145, v154, v155
	v_exp_f32_e32 v152, v76
	v_exp_f32_e32 v153, v77
	v_mfma_f32_32x32x16_bf16 v[48:63], a[236:239], a[140:143], v[48:63]
	ds_read_b64_tr_b16 v[134:135], v208 offset:0x2800
	v_cvt_pk_bf16_f32 v146, v156, v157
	v_mfma_f32_32x32x16_bf16 v[32:47], a[236:239], a[172:175], v[32:47]
	ds_read_b64_tr_b16 v[92:93], v208 offset:0x2200
	v_exp_f32_e32 v154, v78
	v_exp_f32_e32 v155, v79
	ds_read_b64_tr_b16 v[94:95], v208 offset:0x2a00
	v_cvt_pk_bf16_f32 v147, v158, v159
	s_mov_b32 s0, s51
	v_mfma_f32_32x32x16_bf16 v[112:127], a[208:211], a[144:147], v[112:127]
	ds_read_b64_tr_b16 v[88:89], v208 offset:0x2400
	v_cvt_pk_bf16_f32 v84, v80, v81
	v_add_f32_e32 v64, v237, v80
	v_add_f32_e32 v65, v236, v81
	s_add_i32 s1, s17, 0xffffa000
	v_mfma_f32_32x32x16_bf16 v[96:111], a[208:211], a[176:179], v[96:111]
	ds_read_b64_tr_b16 v[90:91], v208 offset:0x2c00
	v_cvt_pk_bf16_f32 v85, v82, v83
	v_add_f32_e32 v64, v64, v82
	v_add_f32_e32 v65, v65, v83
	s_mov_b32 s81, s53
	v_mfma_f32_32x32x16_bf16 v[48:63], a[240:243], a[144:147], v[48:63]
	ds_read_b64_tr_b16 v[80:81], v208 offset:0x2600
	v_cvt_pk_bf16_f32 v86, v240, v241
	v_add_f32_e32 v64, v64, v240
	v_add_f32_e32 v65, v65, v241
	s_add_i32 s82, s17, 0xffffc000
	v_mfma_f32_32x32x16_bf16 v[32:47], a[240:243], a[176:179], v[32:47]
	ds_read_b64_tr_b16 v[82:83], v208 offset:0x2e00
	ds_read_b64_tr_b16 v[76:77], v208 offset:0x3000
	v_cvt_pk_bf16_f32 v87, v242, v243
	v_add_f32_e32 v64, v64, v242
	v_add_f32_e32 v65, v65, v243
	s_mov_b32 s83, s55
	v_mfma_f32_32x32x16_bf16 v[112:127], a[212:215], a[148:151], v[112:127]
	ds_read_b64_tr_b16 v[78:79], v208 offset:0x3800
	v_add_f32_e32 v64, v64, v198
	v_add_f32_e32 v65, v65, v199
	s_add_i32 s84, s17, 0xffffe000
	v_mfma_f32_32x32x16_bf16 v[96:111], a[212:215], a[180:183], v[96:111]
	ds_read_b64_tr_b16 v[72:73], v208 offset:0x3200
	v_add_f32_e32 v64, v64, v230
	v_add_f32_e32 v65, v65, v231
	s_mov_b32 s85, s57
	v_mfma_f32_32x32x16_bf16 v[48:63], a[244:247], a[148:151], v[48:63]
	ds_read_b64_tr_b16 v[74:75], v208 offset:0x3a00
	v_add_f32_e32 v64, v64, v232
	v_add_f32_e32 v65, v65, v233
	s_mov_b32 s86, s17
	v_mfma_f32_32x32x16_bf16 v[32:47], a[244:247], a[180:183], v[32:47]
	ds_read_b64_tr_b16 v[68:69], v208 offset:0x3400
	ds_read_b64_tr_b16 v[70:71], v208 offset:0x3c00
	v_add_f32_e32 v156, v64, v234
	v_add_f32_e32 v157, v65, v235
	s_mov_b32 s87, s31
	v_mfma_f32_32x32x16_bf16 v[112:127], a[216:219], a[152:155], v[112:127]
	ds_read_b64_tr_b16 v[64:65], v208 offset:0x3600
	v_cvt_pk_bf16_f32 v140, v141, v142
	v_add_f32_e32 v158, v238, v141
	v_add_f32_e32 v142, v239, v142
	v_mfma_f32_32x32x16_bf16 v[96:111], a[216:219], a[184:187], v[96:111]
	ds_read_b64_tr_b16 v[66:67], v208 offset:0x3e00
	v_cvt_pk_bf16_f32 v141, v143, v244
	v_add_f32_e32 v143, v158, v143
	v_add_f32_e32 v158, v142, v244
	v_mfma_f32_32x32x16_bf16 v[48:63], a[248:251], a[152:155], v[48:63]
	s_mov_b32 s88, s59
	v_cvt_pk_bf16_f32 v142, v245, v246
	v_add_f32_e32 v159, v143, v245
	v_add_f32_e32 v158, v158, v246
	v_mfma_f32_32x32x16_bf16 v[32:47], a[248:251], a[184:187], v[32:47]
	s_add_i32 s89, s17, 0xfffda080
	v_cvt_pk_bf16_f32 v143, v247, v248
	v_add_f32_e32 v159, v159, v247
	v_add_f32_e32 v158, v158, v248
	v_mfma_f32_32x32x16_bf16 v[112:127], a[220:223], a[156:159], v[112:127]
	s_mov_b32 s90, s61
	v_add_f32_e32 v159, v159, v148
	v_add_f32_e32 v158, v158, v149
	v_mfma_f32_32x32x16_bf16 v[96:111], a[220:223], a[188:191], v[96:111]
	v_add_f32_e32 v159, v159, v150
	v_add_f32_e32 v158, v158, v151
	v_mfma_f32_32x32x16_bf16 v[48:63], a[252:255], a[156:159], v[48:63]
	s_mov_b32 s91, s62
	v_add_f32_e32 v159, v159, v152
	v_add_f32_e32 v158, v158, v153
	v_mfma_f32_32x32x16_bf16 v[32:47], a[252:255], a[188:191], v[32:47]
	s_add_i32 s92, s17, 0xfffde080
	v_add_f32_e32 v159, v159, v154
	v_add_f32_e32 v158, v158, v155
	v_add_f32_e32 v156, v156, v157
	s_waitcnt vmcnt(0) lgkmcnt(0)
	s_barrier
	v_add_f32_e32 v158, v159, v158
	v_mov_b32_e32 v157, v156
	v_mov_b32_e32 v159, v158
	s_nop 0
	v_permlane32_swap_b32_e32 v156, v157
	v_permlane32_swap_b32_e32 v158, v159
	v_add_f32_e32 v156, v156, v157
	v_add_f32_e32 v158, v158, v159
	v_add_f32_e32 v197, v197, v156
	v_add_f32_e32 v196, v196, v158
	s_mov_b32 m0, s0
	v_mfma_f32_32x32x16_bf16 a[0:15], v[180:183], v[164:167], a[0:15]
	buffer_load_dwordx4 v209, s[4:7], s1 offen lds
	s_mov_b32 m0, s81
	v_mfma_f32_32x32x16_bf16 a[16:31], v[180:183], v[192:195], a[16:31]
	buffer_load_dwordx4 v210, s[4:7], s82 offen lds
	s_mov_b32 m0, s83
	v_mfma_f32_32x32x16_bf16 a[32:47], v[184:187], v[164:167], a[32:47]
	buffer_load_dwordx4 v209, s[4:7], s84 offen lds
	s_mov_b32 m0, s85
	v_mfma_f32_32x32x16_bf16 a[48:63], v[184:187], v[192:195], a[48:63]
	buffer_load_dwordx4 v210, s[4:7], s86 offen lds
	s_mov_b32 m0, s87
	v_mfma_f32_32x32x16_bf16 a[64:79], v[176:179], v[164:167], a[64:79]
	buffer_load_dwordx4 v211, s[20:23], s19 offen lds
	s_mov_b32 m0, s88
	v_mfma_f32_32x32x16_bf16 a[80:95], v[176:179], v[192:195], a[80:95]
	buffer_load_dwordx4 v211, s[20:23], s89 offen lds
	s_mov_b32 m0, s90
	v_mfma_f32_32x32x16_bf16 a[96:111], v[188:191], v[164:167], a[96:111]
	buffer_load_dwordx4 v211, s[20:23], s24 offen lds
	s_mov_b32 m0, s91
	v_mfma_f32_32x32x16_bf16 a[112:127], v[188:191], v[192:195], a[112:127]
	buffer_load_dwordx4 v211, s[20:23], s92 offen lds
	v_mfma_f32_32x32x16_bf16 a[0:15], v[172:175], v[128:131], a[0:15]
	v_max3_f32 v156, v112, v113, v48
	v_max3_f32 v157, v114, v115, v49
	v_max3_f32 v156, v156, v50, v51
	v_mfma_f32_32x32x16_bf16 a[16:31], v[172:175], v[144:147], a[16:31]
	ds_read_b128 a[192:195], v204 offset:0
	v_max3_f32 v156, v156, v116, v117
	v_max3_f32 v157, v157, v118, v119
	v_max3_f32 v156, v156, v52, v53
	v_max3_f32 v157, v157, v54, v55
	v_mfma_f32_32x32x16_bf16 a[32:47], v[168:171], v[128:131], a[32:47]
	ds_read_b128 a[196:199], v205 offset:0
	v_max3_f32 v156, v156, v120, v121
	v_max3_f32 v157, v157, v122, v123
	v_max3_f32 v156, v156, v56, v57
	v_max3_f32 v157, v157, v58, v59
	v_mfma_f32_32x32x16_bf16 a[48:63], v[168:171], v[144:147], a[48:63]
	ds_read_b128 a[200:203], v206 offset:0
	v_max3_f32 v156, v156, v124, v125
	v_max3_f32 v157, v157, v126, v127
	v_max3_f32 v156, v156, v60, v61
	v_max3_f32 v157, v157, v62, v63
	v_mfma_f32_32x32x16_bf16 a[64:79], v[160:163], v[128:131], a[64:79]
	ds_read_b128 a[204:207], v207 offset:0
	v_max3_f32 v158, v96, v97, v32
	v_max3_f32 v159, v98, v99, v33
	v_max3_f32 v158, v158, v34, v35
	v_mfma_f32_32x32x16_bf16 a[80:95], v[160:163], v[144:147], a[80:95]
	ds_read_b128 a[208:211], v204 offset:128
	v_max3_f32 v158, v158, v100, v101
	v_max3_f32 v159, v159, v102, v103
	v_max3_f32 v158, v158, v36, v37
	v_max3_f32 v159, v159, v38, v39
	v_mfma_f32_32x32x16_bf16 a[96:111], v[136:139], v[128:131], a[96:111]
	ds_read_b128 a[212:215], v205 offset:128
	v_max3_f32 v128, v158, v104, v105
	v_max3_f32 v129, v159, v106, v107
	v_max3_f32 v128, v128, v40, v41
	v_max3_f32 v129, v129, v42, v43
	v_mfma_f32_32x32x16_bf16 a[112:127], v[136:139], v[144:147], a[112:127]
	ds_read_b128 a[216:219], v206 offset:128
	v_max3_f32 v128, v128, v108, v109
	v_max3_f32 v129, v129, v110, v111
	v_max3_f32 v128, v128, v44, v45
	v_max3_f32 v130, v129, v46, v47
	v_mfma_f32_32x32x16_bf16 a[0:15], v[132:135], v[84:87], a[0:15]
	ds_read_b128 a[220:223], v207 offset:128
	v_max_f32_e32 v129, v156, v157
	v_max_f32_e32 v128, v128, v130
	v_mov_b32_e32 v131, v129
	v_mov_b32_e32 v130, v128
	v_mfma_f32_32x32x16_bf16 a[16:31], v[132:135], v[140:143], a[16:31]
	ds_read_b128 a[224:227], v204 offset:8192
	v_permlane32_swap_b32_e32 v129, v131
	v_permlane32_swap_b32_e32 v128, v130
	v_max_f32_e32 v129, v129, v131
	v_max_f32_e32 v128, v128, v130
	v_max_f32_e32 v130, v129, v128
	v_mfma_f32_32x32x16_bf16 a[32:47], v[92:95], v[84:87], a[32:47]
	ds_read_b128 a[228:231], v205 offset:8192
	v_cmp_lt_f32_e32 vcc, s79, v130
	s_cmp_lg_u64 vcc, 0
	s_cselect_b64 s[0:1], -1, 0
	s_cbranch_vccnz .LBB2_20
.LBB2_16:
	v_cvt_pk_bf16_f32 v156, v198, v199
	v_cvt_pk_bf16_f32 v157, v230, v231
	v_cvt_pk_bf16_f32 v158, v232, v233
	v_cvt_pk_bf16_f32 v159, v234, v235
	v_cvt_pk_bf16_f32 v160, v148, v149
	v_cvt_pk_bf16_f32 v161, v150, v151
	v_cvt_pk_bf16_f32 v162, v152, v153
	v_cvt_pk_bf16_f32 v163, v154, v155
	v_exp_f32_e32 v128, v112
	v_exp_f32_e32 v129, v113
	v_mfma_f32_32x32x16_bf16 a[48:63], v[92:95], v[140:143], a[48:63]
	ds_read_b128 a[232:235], v206 offset:8192
	v_exp_f32_e32 v130, v114
	v_exp_f32_e32 v131, v115
	v_mfma_f32_32x32x16_bf16 a[64:79], v[88:91], v[84:87], a[64:79]
	ds_read_b128 a[236:239], v207 offset:8192
	v_add_f32_e32 v92, v201, v128
	v_add_f32_e32 v93, v201, v129
	v_exp_f32_e32 v132, v116
	v_exp_f32_e32 v133, v117
	v_exp_f32_e32 v134, v118
	v_mfma_f32_32x32x16_bf16 a[80:95], v[88:91], v[140:143], a[80:95]
	ds_read_b128 a[240:243], v204 offset:8320
	v_add_f32_e32 v88, v92, v130
	v_add_f32_e32 v89, v93, v131
	v_exp_f32_e32 v135, v119
	v_exp_f32_e32 v136, v120
	v_mfma_f32_32x32x16_bf16 a[96:111], v[80:83], v[84:87], a[96:111]
	ds_read_b128 a[244:247], v205 offset:8320
	v_add_f32_e32 v84, v88, v132
	v_add_f32_e32 v85, v89, v133
	v_add_f32_e32 v84, v84, v134
	v_exp_f32_e32 v137, v121
	v_exp_f32_e32 v138, v122
	v_exp_f32_e32 v139, v123
	v_mfma_f32_32x32x16_bf16 a[112:127], v[80:83], v[140:143], a[112:127]
	ds_read_b128 a[248:251], v206 offset:8320
	v_add_f32_e32 v80, v85, v135
	v_add_f32_e32 v81, v84, v136
	v_exp_f32_e32 v140, v124
	v_exp_f32_e32 v141, v125
	v_mfma_f32_32x32x16_bf16 a[0:15], v[76:79], v[156:159], a[0:15]
	ds_read_b128 a[252:255], v207 offset:8320
	v_add_f32_e32 v80, v80, v137
	v_add_f32_e32 v81, v81, v138
	v_add_f32_e32 v80, v80, v139
	v_exp_f32_e32 v142, v126
	v_exp_f32_e32 v143, v127
	v_exp_f32_e32 v144, v96
	v_mfma_f32_32x32x16_bf16 a[16:31], v[76:79], v[160:163], a[16:31]
	v_add_f32_e32 v76, v81, v140
	v_add_f32_e32 v77, v80, v141
	v_exp_f32_e32 v145, v97
	v_exp_f32_e32 v146, v98
	v_mfma_f32_32x32x16_bf16 a[32:47], v[72:75], v[156:159], a[32:47]
	v_add_f32_e32 v239, v76, v142
	v_add_f32_e32 v238, v77, v143
	v_add_f32_e32 v76, v201, v144
	v_exp_f32_e32 v147, v99
	v_exp_f32_e32 v148, v100
	v_exp_f32_e32 v149, v101
	v_mfma_f32_32x32x16_bf16 a[48:63], v[72:75], v[160:163], a[48:63]
	v_add_f32_e32 v72, v201, v145
	v_add_f32_e32 v73, v76, v146
	v_exp_f32_e32 v150, v102
	v_exp_f32_e32 v151, v103
	v_mfma_f32_32x32x16_bf16 a[64:79], v[68:71], v[156:159], a[64:79]
	v_add_f32_e32 v72, v72, v147
	v_add_f32_e32 v73, v73, v148
	v_add_f32_e32 v72, v72, v149
	v_exp_f32_e32 v152, v104
	v_exp_f32_e32 v153, v105
	v_exp_f32_e32 v154, v106
	v_mfma_f32_32x32x16_bf16 a[80:95], v[68:71], v[160:163], a[80:95]
	v_add_f32_e32 v68, v73, v150
	v_add_f32_e32 v69, v72, v151
	v_mfma_f32_32x32x16_bf16 a[96:111], v[64:67], v[156:159], a[96:111]
	v_exp_f32_e32 v155, v107
	v_exp_f32_e32 v156, v108
	v_add_f32_e32 v68, v68, v152
	v_add_f32_e32 v69, v69, v153
	v_add_f32_e32 v68, v68, v154
	v_exp_f32_e32 v157, v109
	v_exp_f32_e32 v158, v110
	v_exp_f32_e32 v159, v111
	v_mfma_f32_32x32x16_bf16 a[112:127], v[64:67], v[160:163], a[112:127]
	v_add_f32_e32 v64, v69, v155
	v_add_f32_e32 v65, v68, v156
	s_andn2_b64 vcc, exec, s[0:1]
	v_add_f32_e32 v64, v64, v157
	v_add_f32_e32 v240, v65, v158
	s_nop 0
	v_add_f32_e32 v241, v64, v159
	s_cbranch_vccz .LBB2_21
